# attention loop software-pipelined: QK of tile t+1 interleaved with PV of tile t, softmax VALU spread evenly over the MFMA stream
# speedup vs baseline: 1.0145x; 1.0120x over previous
.LBB0_733:
	s_or_b64 exec, exec, s[8:9]
	s_movk_i32 s4, 0xf0
	s_cmp_lg_u32 0, -1
	v_lshlrev_b32_e32 v39, 8, v141
	v_bitop3_b32 v80, v142, s4, v136 bitop3:0x48
	s_cselect_b32 s10, 0, 0
	v_cvt_pk_bf16_f32 v96, v134, v135
	v_cvt_pk_bf16_f32 v97, v132, v133
	v_cvt_pk_bf16_f32 v98, v130, v131
	v_cvt_pk_bf16_f32 v99, v128, v129
	v_cvt_pk_bf16_f32 v100, v126, v127
	v_cvt_pk_bf16_f32 v101, v124, v125
	v_cvt_pk_bf16_f32 v102, v122, v123
	v_cvt_pk_bf16_f32 v103, v120, v121
	v_cvt_pk_bf16_f32 v104, v70, v71
	v_cvt_pk_bf16_f32 v105, v74, v75
	v_cvt_pk_bf16_f32 v106, v64, v65
	v_cvt_pk_bf16_f32 v107, v68, v69
	v_cvt_pk_bf16_f32 v108, v60, v61
	v_cvt_pk_bf16_f32 v109, v66, v67
	v_cvt_pk_bf16_f32 v110, v56, v57
	v_cvt_pk_bf16_f32 v111, v58, v59
	v_cvt_pk_bf16_f32 v112, v112, v113
	v_cvt_pk_bf16_f32 v113, v118, v119
	v_cvt_pk_bf16_f32 v114, v114, v115
	v_cvt_pk_bf16_f32 v115, v116, v117
	v_cvt_pk_bf16_f32 v116, v78, v79
	v_cvt_pk_bf16_f32 v117, v76, v77
	v_cvt_pk_bf16_f32 v118, v72, v73
	v_cvt_pk_bf16_f32 v119, v62, v63
	v_cvt_pk_bf16_f32 v120, v52, v53
	v_cvt_pk_bf16_f32 v121, v54, v55
	v_cvt_pk_bf16_f32 v122, v46, v47
	v_cvt_pk_bf16_f32 v123, v50, v51
	v_cvt_pk_bf16_f32 v124, v44, v45
	v_cvt_pk_bf16_f32 v125, v48, v49
	v_cvt_pk_bf16_f32 v126, v40, v41
	v_cvt_pk_bf16_f32 v127, v42, v43
	v_readlane_b32 s100, v250, 8
	v_mbcnt_lo_u32_b32 v68, -1, 0
	v_mbcnt_hi_u32_b32 v68, -1, v68
	s_nop 1
	v_add_u32_e32 v69, s100, v68
	v_lshrrev_b32_e32 v70, 3, v69
	v_and_b32_e32 v71, 7, v69
	v_lshrrev_b32_e32 v72, 2, v71
	v_bfe_u32 v73, v71, 1, 1
	v_and_b32_e32 v74, 1, v71
	v_lshlrev_b32_e32 v74, 1, v74
	v_lshl_add_u32 v75, v72, 2, v74
	v_bfe_u32 v76, v70, 1, 3
	v_xor_b32_e32 v77, v75, v76
	v_add_u32_e32 v78, 1, v75
	v_xor_b32_e32 v78, v78, v76
	v_lshlrev_b32_e32 v79, 7, v70
	v_lshl_add_u32 v79, v73, 3, v79
	v_lshl_add_u32 v64, v77, 4, v79
	v_lshl_add_u32 v65, v78, 4, v79
	v_add_u32_e32 v66, 0x2000, v64
	v_add_u32_e32 v67, 0x2000, v65
	v_or_b32_e32 v81, v39, v80
	s_add_i32 s15, s10, 0x10000
	v_and_b32_e32 v82, 6, v137
	v_lshrrev_b32_e32 v84, 4, v136
	s_waitcnt vmcnt(0)
	s_waitcnt vmcnt(0)
	s_add_i32 s11, s10, 0x12000
	v_lshl_add_u32 v83, v139, 7, s10
	v_bitop3_b32 v85, v84, v82, 7 bitop3:0x6c
	v_and_b32_e32 v86, 8, v138
	v_or_b32_e32 v82, 1, v82
	v_add_u32_e32 v225, s15, v81
	s_waitcnt vmcnt(4)
	ds_write_b128 v225, v[24:27] offset:0
	v_lshlrev_b32_e32 v85, 4, v85
	v_add_u32_e32 v87, v83, v86
	v_bitop3_b32 v82, v84, v82, 7 bitop3:0x6c
	v_add3_u32 v226, v80, s11, v39
	ds_write_b128 v226, v[28:31] offset:0
	v_lshlrev_b32_e32 v82, 4, v82
	v_add_u32_e32 v227, v87, v85
	ds_write_b64 v64, v[12:13] offset:0
	v_lshrrev_b32_e32 v32, 5, v136
	v_add_u32_e32 v83, 0x2000, v83
	v_or_b32_e32 v84, v85, v86
	v_add_u32_e32 v228, v87, v82
	ds_write_b64 v65, v[14:15] offset:0
	v_xor_b32_e32 v32, v32, v137
	v_or_b32_e32 v86, v82, v86
	v_add_u32_e32 v229, v84, v83
	ds_write_b64 v66, v[4:5] offset:0
	v_lshlrev_b32_e32 v32, 4, v32
	v_add_u32_e32 v184, v86, v83
	ds_write_b64 v67, v[6:7] offset:0
	v_lshlrev_b32_e32 v33, 8, v143
	v_and_b32_e32 v32, 16, v32
	v_bfe_u32 v35, v137, 1, 3
	s_waitcnt vmcnt(4)
	ds_write_b128 v225, v[20:23] offset:0x4000
	v_lshlrev_b32_e32 v36, 5, v35
	v_add3_u32 v32, v33, s15, v32
	s_movk_i32 s16, 0x60
	ds_write_b128 v226, v[16:19] offset:0x4000
	v_xad_u32 v204, v36, s16, v32
	s_movk_i32 s16, 0x80
	ds_write_b64 v64, v[8:9] offset:0x4000
	v_xad_u32 v205, v36, s16, v32
	s_movk_i32 s16, 0xa0
	ds_write_b64 v65, v[10:11] offset:0x4000
	s_add_u32 s8, s6, 0x100
	v_xad_u32 v206, v36, s16, v32
	s_movk_i32 s16, 0xc0
	ds_write_b64 v66, v[0:1] offset:0x4000
	s_addc_u32 s9, s7, 0
	v_xad_u32 v207, v36, s16, v32
	s_movk_i32 s16, 0xe0
	ds_write_b64 v67, v[2:3] offset:0x4000
	v_add_u32_e32 v201, v32, v36
	v_xad_u32 v202, v36, 32, v32
	v_xad_u32 v203, v36, 64, v32
	v_xad_u32 v208, v36, s16, v32
	v_lshl_add_u32 v32, v143, 7, s10
	s_add_u32 s10, s78, 0x20000
	global_load_dwordx4 v[132:135], v198, s[8:9]
	s_addc_u32 s11, s79, 0
	global_load_dwordx4 v[128:131], v199, s[8:9]
	v_lshrrev_b32_e32 v34, 1, v137
	global_load_dwordx4 v[136:139], v196, s[10:11]
	s_add_u32 s6, s6, 0x180
	v_bitop3_b32 v34, v140, v34, 7 bitop3:0x78
	v_bitop3_b32 v37, v140, v35, 2 bitop3:0x36
	v_bitop3_b32 v38, v140, v35, 4 bitop3:0x36
	v_bitop3_b32 v35, v140, v35, 6 bitop3:0x36
	global_load_dwordx4 v[140:143], v197, s[10:11]
	s_addc_u32 s7, s7, 0
	s_add_u32 s8, s78, 0x30000
	global_load_dwordx4 v[148:151], v198, s[6:7]
	s_addc_u32 s9, s79, 0
	global_load_dwordx4 v[144:147], v199, s[6:7]
	global_load_dwordx4 v[152:155], v196, s[8:9]
	s_add_u32 s10, s13, s14
	global_load_dwordx4 v[156:159], v197, s[8:9]
	s_addc_u32 s11, s12, 0
	s_add_u32 s12, s41, s30
	v_mov_b32_e32 v0, 0
	s_mov_b32 s4, 0
	v_lshl_add_u32 v209, v34, 4, v32
	v_lshl_add_u32 v210, v37, 4, v32
	v_lshl_add_u32 v211, v38, 4, v32
	v_lshl_add_u32 v224, v35, 4, v32
	s_addc_u32 s13, 0, s31
	v_mov_b32_e32 v1, v0
	v_mov_b32_e32 v2, v0
	v_mov_b32_e32 v3, v0
	v_mov_b32_e32 v4, v0
	v_mov_b32_e32 v5, v0
	v_mov_b32_e32 v6, v0
	v_mov_b32_e32 v7, v0
	v_mov_b32_e32 v8, v0
	v_mov_b32_e32 v9, v0
	v_mov_b32_e32 v10, v0
	v_mov_b32_e32 v11, v0
	v_mov_b32_e32 v12, v0
	v_mov_b32_e32 v13, v0
	v_mov_b32_e32 v14, v0
	v_mov_b32_e32 v15, v0
	v_mov_b32_e32 v16, v0
	v_mov_b32_e32 v17, v0
	v_mov_b32_e32 v18, v0
	v_mov_b32_e32 v19, v0
	v_mov_b32_e32 v20, v0
	v_mov_b32_e32 v21, v0
	v_mov_b32_e32 v22, v0
	v_mov_b32_e32 v23, v0
	v_mov_b32_e32 v24, v0
	v_mov_b32_e32 v25, v0
	v_mov_b32_e32 v26, v0
	v_mov_b32_e32 v27, v0
	v_mov_b32_e32 v28, v0
	v_mov_b32_e32 v29, v0
	v_mov_b32_e32 v30, v0
	v_mov_b32_e32 v31, v0
	v_mov_b32_e32 v32, v0
	v_mov_b32_e32 v33, v0
	v_mov_b32_e32 v34, v0
	v_mov_b32_e32 v35, v0
	v_mov_b32_e32 v36, v0
	v_mov_b32_e32 v37, v0
	v_mov_b32_e32 v38, v0
	v_mov_b32_e32 v39, v0
	v_mov_b32_e32 v40, v0
	v_mov_b32_e32 v41, v0
	v_mov_b32_e32 v42, v0
	v_mov_b32_e32 v43, v0
	v_mov_b32_e32 v44, v0
	v_mov_b32_e32 v45, v0
	v_mov_b32_e32 v46, v0
	v_mov_b32_e32 v47, v0
	v_mov_b32_e32 v48, v0
	v_mov_b32_e32 v49, v0
	v_mov_b32_e32 v50, v0
	v_mov_b32_e32 v51, v0
	v_mov_b32_e32 v52, v0
	v_mov_b32_e32 v53, v0
	v_mov_b32_e32 v54, v0
	v_mov_b32_e32 v55, v0
	v_mov_b32_e32 v56, v0
	v_mov_b32_e32 v57, v0
	v_mov_b32_e32 v58, v0
	v_mov_b32_e32 v59, v0
	v_mov_b32_e32 v60, v0
	v_mov_b32_e32 v61, v0
	v_mov_b32_e32 v62, v0
	v_mov_b32_e32 v63, v0
	v_mov_b32_e32 v160, v0
	v_mov_b32_e32 v161, v0
	v_mov_b32_e32 v227, v64
	v_mov_b32_e32 v228, v65
	v_mov_b32_e32 v229, v66
	v_mov_b32_e32 v184, v67
	v_readlane_b32 s100, v250, 8
	v_mbcnt_lo_u32_b32 v68, -1, 0
	v_mbcnt_hi_u32_b32 v68, -1, v68
	v_and_b32_e32 v69, 15, v68
	v_lshrrev_b32_e32 v70, 4, v68
	v_lshlrev_b32_e32 v72, 8, v69
	v_add_u32_e32 v72, 0x10000, v72
	v_add_u32_e32 v71, 0, v70
	v_xor_b32_e32 v71, v71, v69
	v_lshl_add_u32 v201, v71, 4, v72
	v_add_u32_e32 v71, 4, v70
	v_xor_b32_e32 v71, v71, v69
	v_lshl_add_u32 v202, v71, 4, v72
	v_add_u32_e32 v71, 8, v70
	v_xor_b32_e32 v71, v71, v69
	v_lshl_add_u32 v203, v71, 4, v72
	v_add_u32_e32 v71, 12, v70
	v_xor_b32_e32 v71, v71, v69
	v_lshl_add_u32 v246, v71, 4, v72
	v_bfe_u32 v73, v69, 1, 3
	v_lshlrev_b32_e32 v76, 7, v69
	v_add_u32_e32 v71, 0, v70
	v_xor_b32_e32 v71, v71, v73
	v_lshl_add_u32 v209, v71, 4, v76
	v_add_u32_e32 v71, 4, v70
	v_xor_b32_e32 v71, v71, v73
	v_lshl_add_u32 v210, v71, 4, v76
	s_lshl_b32 s101, s100, 7
	s_add_u32 s101, s101, 0x8000
	s_cmpk_ge_u32 s100, 0x100
	s_cselect_b32 s6, 0x8000, 0
	s_add_u32 s101, s101, s6
	v_and_b32_e32 v74, 31, v68
	v_lshrrev_b32_e32 v75, 5, v68
	v_lshlrev_b32_e32 v74, 8, v74
	v_lshl_add_u32 v74, v75, 4, v74
	v_add_u32_e32 v74, s101, v74
	v_lshlrev_b32_e32 v75, 8, v69
	v_lshl_add_u32 v75, v70, 4, v75
	v_add_u32_e32 v75, s101, v75
	ds_write_b128 v74, v[96:99] offset:0
	ds_write_b128 v74, v[100:103] offset:32
	ds_write_b128 v74, v[104:107] offset:64
	ds_write_b128 v74, v[108:111] offset:96
	ds_write_b128 v74, v[112:115] offset:128
	ds_write_b128 v74, v[116:119] offset:160
	ds_write_b128 v74, v[120:123] offset:192
	ds_write_b128 v74, v[124:127] offset:224
	s_waitcnt lgkmcnt(0)
	ds_read_b128 v[96:99], v75 offset:0
	ds_read_b128 v[100:103], v75 offset:64
	ds_read_b128 v[104:107], v75 offset:128
	ds_read_b128 v[108:111], v75 offset:192
	ds_read_b128 v[112:115], v75 offset:4096
	ds_read_b128 v[116:119], v75 offset:4160
	ds_read_b128 v[120:123], v75 offset:4224
	ds_read_b128 v[124:127], v75 offset:4288
	s_waitcnt vmcnt(0)
	s_waitcnt lgkmcnt(0)
	s_barrier
	ds_write_b128 v225, v[136:139] offset:32768
	ds_write_b128 v226, v[140:143] offset:32768
	s_add_u32 s15, s22, s12
	s_addc_u32 s14, s23, s13
	s_add_u32 s6, s15, 0x23a40000
	s_addc_u32 s7, s14, 0
	s_waitcnt lgkmcnt(0)
	global_load_dwordx4 v[136:139], v196, s[6:7]
	global_load_dwordx4 v[140:143], v197, s[6:7]
	v_mov_b32_e32 v194, 0
	v_mov_b32_e32 v195, 0
	s_barrier
	ds_read_b128 v[160:163], v201 offset:0
	ds_read_b128 v[164:167], v202 offset:0
	ds_read_b128 v[168:171], v203 offset:0
	ds_read_b128 v[172:175], v246 offset:0
	ds_read_b128 v[176:179], v201 offset:4096
	ds_read_b128 v[180:183], v202 offset:4096
	ds_read_b128 v[230:233], v203 offset:4096
	s_waitcnt lgkmcnt(6)
	v_mfma_f32_16x16x32_bf16 v[64:67], v[160:163], v[96:99], 0
	v_mfma_f32_16x16x32_bf16 v[68:71], v[160:163], v[112:115], 0
	ds_read_b128 v[234:237], v246 offset:4096
	s_waitcnt lgkmcnt(6)
	v_mfma_f32_16x16x32_bf16 v[68:71], v[164:167], v[116:119], v[68:71]
	v_mfma_f32_16x16x32_bf16 v[64:67], v[164:167], v[100:103], v[64:67]
	ds_read_b128 v[160:163], v201 offset:8192
	s_waitcnt lgkmcnt(6)
	v_mfma_f32_16x16x32_bf16 v[64:67], v[168:171], v[104:107], v[64:67]
	v_mfma_f32_16x16x32_bf16 v[68:71], v[168:171], v[120:123], v[68:71]
	ds_read_b128 v[164:167], v202 offset:8192
	s_waitcnt lgkmcnt(6)
	v_mfma_f32_16x16x32_bf16 v[68:71], v[172:175], v[124:127], v[68:71]
	v_mfma_f32_16x16x32_bf16 v[64:67], v[172:175], v[108:111], v[64:67]
	ds_read_b128 v[168:171], v203 offset:8192
	s_waitcnt lgkmcnt(6)
	v_mfma_f32_16x16x32_bf16 v[72:75], v[176:179], v[96:99], 0
	s_nop 7
	s_nop 1
	v_exp_f32_e32 v64, v64
	v_exp_f32_e32 v68, v68
	v_mfma_f32_16x16x32_bf16 v[76:79], v[176:179], v[112:115], 0
	v_exp_f32_e32 v65, v65
	v_exp_f32_e32 v69, v69
	ds_read_b128 v[172:175], v246 offset:8192
	s_waitcnt lgkmcnt(6)
	v_mfma_f32_16x16x32_bf16 v[76:79], v[180:183], v[116:119], v[76:79]
	v_exp_f32_e32 v66, v66
	v_exp_f32_e32 v70, v70
	v_mfma_f32_16x16x32_bf16 v[72:75], v[180:183], v[100:103], v[72:75]
	v_exp_f32_e32 v67, v67
	v_exp_f32_e32 v71, v71
	ds_read_b128 v[176:179], v201 offset:12288
	s_waitcnt lgkmcnt(6)
	v_mfma_f32_16x16x32_bf16 v[72:75], v[230:233], v[104:107], v[72:75]
	v_add_f32_e32 v220, v64, v65
	v_add_f32_e32 v221, v68, v69
	v_mfma_f32_16x16x32_bf16 v[76:79], v[230:233], v[120:123], v[76:79]
	v_add_f32_e32 v220, v220, v66
	v_add_f32_e32 v221, v221, v70
	ds_read_b128 v[180:183], v202 offset:12288
	s_waitcnt lgkmcnt(6)
	v_mfma_f32_16x16x32_bf16 v[76:79], v[234:237], v[124:127], v[76:79]
	v_add_f32_e32 v220, v220, v67
	v_mfma_f32_16x16x32_bf16 v[72:75], v[234:237], v[108:111], v[72:75]
	v_add_f32_e32 v221, v221, v71
	ds_read_b128 v[230:233], v203 offset:12288
	s_waitcnt lgkmcnt(6)
	v_mfma_f32_16x16x32_bf16 v[80:83], v[160:163], v[96:99], 0
	s_nop 7
	s_nop 1
	v_exp_f32_e32 v72, v72
	v_exp_f32_e32 v76, v76
	v_exp_f32_e32 v73, v73
	v_mfma_f32_16x16x32_bf16 v[84:87], v[160:163], v[112:115], 0
	v_exp_f32_e32 v77, v77
	v_exp_f32_e32 v74, v74
	v_exp_f32_e32 v78, v78
	ds_read_b128 v[234:237], v246 offset:12288
	s_waitcnt lgkmcnt(6)
	v_mfma_f32_16x16x32_bf16 v[84:87], v[164:167], v[116:119], v[84:87]
	v_exp_f32_e32 v75, v75
	v_exp_f32_e32 v79, v79
	v_add_f32_e32 v220, v220, v72
	v_mfma_f32_16x16x32_bf16 v[80:83], v[164:167], v[100:103], v[80:83]
	v_add_f32_e32 v221, v221, v76
	v_add_f32_e32 v220, v220, v73
	v_add_f32_e32 v221, v221, v77
	s_waitcnt lgkmcnt(5)
	v_mfma_f32_16x16x32_bf16 v[80:83], v[168:171], v[104:107], v[80:83]
	v_add_f32_e32 v220, v220, v74
	v_add_f32_e32 v221, v221, v78
	v_add_f32_e32 v220, v220, v75
	v_mfma_f32_16x16x32_bf16 v[84:87], v[168:171], v[120:123], v[84:87]
	v_add_f32_e32 v221, v221, v79
	v_cvt_pk_bf16_f32 v216, v64, v65
	v_cvt_pk_bf16_f32 v217, v66, v67
	s_waitcnt lgkmcnt(4)
	v_mfma_f32_16x16x32_bf16 v[84:87], v[172:175], v[124:127], v[84:87]
	v_cvt_pk_bf16_f32 v238, v68, v69
	v_cvt_pk_bf16_f32 v239, v70, v71
	v_cvt_pk_bf16_f32 v218, v72, v73
	v_mfma_f32_16x16x32_bf16 v[80:83], v[172:175], v[108:111], v[80:83]
	v_cvt_pk_bf16_f32 v219, v74, v75
	v_cvt_pk_bf16_f32 v240, v76, v77
	v_cvt_pk_bf16_f32 v241, v78, v79
	s_waitcnt lgkmcnt(3)
	v_mfma_f32_16x16x32_bf16 v[88:91], v[176:179], v[96:99], 0
	s_nop 7
	s_nop 1
	v_exp_f32_e32 v80, v80
	v_exp_f32_e32 v84, v84
	v_mfma_f32_16x16x32_bf16 v[92:95], v[176:179], v[112:115], 0
	v_exp_f32_e32 v81, v81
	v_exp_f32_e32 v85, v85
	s_waitcnt lgkmcnt(2)
	v_mfma_f32_16x16x32_bf16 v[92:95], v[180:183], v[116:119], v[92:95]
	v_exp_f32_e32 v82, v82
	v_exp_f32_e32 v86, v86
	v_mfma_f32_16x16x32_bf16 v[88:91], v[180:183], v[100:103], v[88:91]
	v_exp_f32_e32 v83, v83
	v_exp_f32_e32 v87, v87
	s_waitcnt lgkmcnt(1)
	v_mfma_f32_16x16x32_bf16 v[88:91], v[230:233], v[104:107], v[88:91]
	v_add_f32_e32 v220, v220, v80
	v_add_f32_e32 v221, v221, v84
	v_mfma_f32_16x16x32_bf16 v[92:95], v[230:233], v[120:123], v[92:95]
	v_add_f32_e32 v220, v220, v81
	v_add_f32_e32 v221, v221, v85
	s_waitcnt lgkmcnt(0)
	v_mfma_f32_16x16x32_bf16 v[92:95], v[234:237], v[124:127], v[92:95]
	v_add_f32_e32 v220, v220, v82
	v_add_f32_e32 v221, v221, v86
	v_mfma_f32_16x16x32_bf16 v[88:91], v[234:237], v[108:111], v[88:91]
	v_add_f32_e32 v220, v220, v83
	v_add_f32_e32 v221, v221, v87
.LBB0_734:
	s_waitcnt lgkmcnt(0)
	s_barrier
	ds_read_b128 v[160:163], v201 offset:16384
	ds_read_b128 v[164:167], v209 offset:0
	ds_read_b128 v[168:171], v202 offset:16384
	ds_read_b128 v[172:175], v209 offset:2048
	ds_read_b128 v[176:179], v203 offset:16384
	ds_read_b128 v[180:183], v209 offset:4096
	ds_read_b128 v[230:233], v246 offset:16384
	s_waitcnt lgkmcnt(6)
	v_mfma_f32_16x16x32_bf16 v[64:67], v[160:163], v[96:99], 0
	v_exp_f32_e32 v88, v88
	v_exp_f32_e32 v92, v92
	v_mfma_f32_16x16x32_bf16 v[68:71], v[160:163], v[112:115], 0
	v_exp_f32_e32 v89, v89
	v_exp_f32_e32 v93, v93
	ds_read_b128 v[234:237], v209 offset:6144
	s_add_u32 s16, s22, s10
	s_addc_u32 s17, s23, s11
	s_add_u32 s15, s22, s12
	s_addc_u32 s14, s23, s13
	s_add_u32 s8, s16, 0x3bc00200
	s_addc_u32 s9, s17, 0
	s_add_u32 s6, s15, 0x23a50000
	s_addc_u32 s7, s14, 0
	s_waitcnt lgkmcnt(6)
	v_mfma_f32_16x16x32_bf16 v[0:3], v[164:167], v[216:219], v[0:3]
	v_exp_f32_e32 v90, v90
	v_exp_f32_e32 v94, v94
	v_mfma_f32_16x16x32_bf16 v[4:7], v[164:167], v[238:241], v[4:7]
	v_exp_f32_e32 v91, v91
	v_exp_f32_e32 v95, v95
	ds_read_b128 v[160:163], v201 offset:20480
	s_waitcnt vmcnt(4)
	ds_write_b128 v225, v[152:155] offset:49152
	s_waitcnt lgkmcnt(7)
	v_mfma_f32_16x16x32_bf16 v[68:71], v[168:171], v[116:119], v[68:71]
	v_add_f32_e32 v220, v220, v88
	v_add_f32_e32 v221, v221, v92
	v_mfma_f32_16x16x32_bf16 v[64:67], v[168:171], v[100:103], v[64:67]
	v_add_f32_e32 v220, v220, v89
	v_add_f32_e32 v221, v221, v93
	ds_read_b128 v[164:167], v209 offset:8192
	ds_write_b128 v226, v[156:159] offset:49152
	s_waitcnt lgkmcnt(8)
	v_mfma_f32_16x16x32_bf16 v[12:15], v[172:175], v[238:241], v[12:15]
	v_add_f32_e32 v220, v220, v90
	v_add_f32_e32 v221, v221, v94
	v_mfma_f32_16x16x32_bf16 v[8:11], v[172:175], v[216:219], v[8:11]
	v_add_f32_e32 v220, v220, v91
	v_add_f32_e32 v221, v221, v95
	ds_read_b128 v[168:171], v202 offset:20480
	ds_write_b64 v227, v[132:133] offset:32768
	s_waitcnt lgkmcnt(9)
	v_mfma_f32_16x16x32_bf16 v[64:67], v[176:179], v[104:107], v[64:67]
	v_add_f32_e32 v194, v194, v220
	v_add_f32_e32 v195, v195, v221
	v_mfma_f32_16x16x32_bf16 v[68:71], v[176:179], v[120:123], v[68:71]
	v_cvt_pk_bf16_f32 v242, v80, v81
	v_cvt_pk_bf16_f32 v243, v82, v83
	ds_read_b128 v[172:175], v209 offset:10240
	ds_write_b64 v228, v[134:135] offset:32768
	s_waitcnt lgkmcnt(10)
	v_mfma_f32_16x16x32_bf16 v[16:19], v[180:183], v[216:219], v[16:19]
	v_cvt_pk_bf16_f32 v204, v84, v85
	v_mfma_f32_16x16x32_bf16 v[20:23], v[180:183], v[238:241], v[20:23]
	v_cvt_pk_bf16_f32 v205, v86, v87
	ds_read_b128 v[176:179], v203 offset:20480
	ds_write_b64 v229, v[128:129] offset:32768
	s_waitcnt lgkmcnt(11)
	v_mfma_f32_16x16x32_bf16 v[68:71], v[230:233], v[124:127], v[68:71]
	v_cvt_pk_bf16_f32 v244, v88, v89
	v_mfma_f32_16x16x32_bf16 v[64:67], v[230:233], v[108:111], v[64:67]
	v_cvt_pk_bf16_f32 v245, v90, v91
	ds_read_b128 v[180:183], v209 offset:12288
	ds_write_b64 v184, v[130:131] offset:32768
	s_waitcnt lgkmcnt(12)
	v_mfma_f32_16x16x32_bf16 v[28:31], v[234:237], v[238:241], v[28:31]
	v_cvt_pk_bf16_f32 v206, v92, v93
	v_mfma_f32_16x16x32_bf16 v[24:27], v[234:237], v[216:219], v[24:27]
	v_cvt_pk_bf16_f32 v207, v94, v95
	ds_read_b128 v[230:233], v246 offset:20480
	global_load_dwordx4 v[132:135], v198, s[8:9]
	s_waitcnt lgkmcnt(12)
	v_mfma_f32_16x16x32_bf16 v[72:75], v[160:163], v[96:99], 0
	v_exp_f32_e32 v64, v64
	v_mfma_f32_16x16x32_bf16 v[76:79], v[160:163], v[112:115], 0
	v_exp_f32_e32 v68, v68
	ds_read_b128 v[234:237], v209 offset:14336
	global_load_dwordx4 v[128:131], v199, s[8:9]
	s_waitcnt lgkmcnt(11)
	v_mfma_f32_16x16x32_bf16 v[32:35], v[164:167], v[216:219], v[32:35]
	v_exp_f32_e32 v65, v65
	v_mfma_f32_16x16x32_bf16 v[36:39], v[164:167], v[238:241], v[36:39]
	v_exp_f32_e32 v69, v69
	ds_read_b128 v[160:163], v201 offset:24576
	global_load_dwordx4 v[152:155], v196, s[6:7]
	s_waitcnt lgkmcnt(10)
	v_mfma_f32_16x16x32_bf16 v[76:79], v[168:171], v[116:119], v[76:79]
	v_exp_f32_e32 v66, v66
	v_mfma_f32_16x16x32_bf16 v[72:75], v[168:171], v[100:103], v[72:75]
	v_exp_f32_e32 v70, v70
	ds_read_b128 v[164:167], v210 offset:0
	global_load_dwordx4 v[156:159], v197, s[6:7]
	s_waitcnt lgkmcnt(9)
	v_mfma_f32_16x16x32_bf16 v[44:47], v[172:175], v[238:241], v[44:47]
	v_exp_f32_e32 v67, v67
	v_mfma_f32_16x16x32_bf16 v[40:43], v[172:175], v[216:219], v[40:43]
	v_exp_f32_e32 v71, v71
	ds_read_b128 v[168:171], v202 offset:24576
	s_waitcnt lgkmcnt(8)
	v_mfma_f32_16x16x32_bf16 v[72:75], v[176:179], v[104:107], v[72:75]
	v_add_f32_e32 v220, v64, v65
	v_mfma_f32_16x16x32_bf16 v[76:79], v[176:179], v[120:123], v[76:79]
	v_add_f32_e32 v221, v68, v69
	ds_read_b128 v[172:175], v210 offset:2048
	s_waitcnt lgkmcnt(7)
	v_mfma_f32_16x16x32_bf16 v[48:51], v[180:183], v[216:219], v[48:51]
	v_add_f32_e32 v220, v220, v66
	v_mfma_f32_16x16x32_bf16 v[52:55], v[180:183], v[238:241], v[52:55]
	v_add_f32_e32 v221, v221, v70
	ds_read_b128 v[176:179], v203 offset:24576
	s_waitcnt lgkmcnt(6)
	v_mfma_f32_16x16x32_bf16 v[76:79], v[230:233], v[124:127], v[76:79]
	v_add_f32_e32 v220, v220, v67
	v_mfma_f32_16x16x32_bf16 v[72:75], v[230:233], v[108:111], v[72:75]
	v_add_f32_e32 v221, v221, v71
	ds_read_b128 v[180:183], v210 offset:4096
	s_waitcnt lgkmcnt(6)
	v_mfma_f32_16x16x32_bf16 v[60:63], v[234:237], v[238:241], v[60:63]
	v_mfma_f32_16x16x32_bf16 v[56:59], v[234:237], v[216:219], v[56:59]
	ds_read_b128 v[230:233], v246 offset:24576
	s_waitcnt lgkmcnt(6)
	v_mfma_f32_16x16x32_bf16 v[80:83], v[160:163], v[96:99], 0
	v_exp_f32_e32 v72, v72
	v_exp_f32_e32 v76, v76
	v_mfma_f32_16x16x32_bf16 v[84:87], v[160:163], v[112:115], 0
	v_exp_f32_e32 v73, v73
	v_exp_f32_e32 v77, v77
	ds_read_b128 v[234:237], v210 offset:6144
	s_waitcnt lgkmcnt(6)
	v_mfma_f32_16x16x32_bf16 v[0:3], v[164:167], v[242:245], v[0:3]
	v_exp_f32_e32 v74, v74
	v_exp_f32_e32 v78, v78
	v_mfma_f32_16x16x32_bf16 v[4:7], v[164:167], v[204:207], v[4:7]
	v_exp_f32_e32 v75, v75
	v_exp_f32_e32 v79, v79
	ds_read_b128 v[160:163], v201 offset:28672
	s_waitcnt lgkmcnt(6)
	v_mfma_f32_16x16x32_bf16 v[84:87], v[168:171], v[116:119], v[84:87]
	v_add_f32_e32 v220, v220, v72
	v_add_f32_e32 v221, v221, v76
	v_mfma_f32_16x16x32_bf16 v[80:83], v[168:171], v[100:103], v[80:83]
	v_add_f32_e32 v220, v220, v73
	v_add_f32_e32 v221, v221, v77
	ds_read_b128 v[164:167], v210 offset:8192
	s_waitcnt lgkmcnt(6)
	v_mfma_f32_16x16x32_bf16 v[12:15], v[172:175], v[204:207], v[12:15]
	v_add_f32_e32 v220, v220, v74
	v_add_f32_e32 v221, v221, v78
	v_mfma_f32_16x16x32_bf16 v[8:11], v[172:175], v[242:245], v[8:11]
	v_add_f32_e32 v220, v220, v75
	v_add_f32_e32 v221, v221, v79
	ds_read_b128 v[168:171], v202 offset:28672
	s_waitcnt lgkmcnt(6)
	v_mfma_f32_16x16x32_bf16 v[80:83], v[176:179], v[104:107], v[80:83]
	v_cvt_pk_bf16_f32 v216, v64, v65
	v_mfma_f32_16x16x32_bf16 v[84:87], v[176:179], v[120:123], v[84:87]
	v_cvt_pk_bf16_f32 v217, v66, v67
	ds_read_b128 v[172:175], v210 offset:10240
	s_waitcnt lgkmcnt(6)
	v_mfma_f32_16x16x32_bf16 v[16:19], v[180:183], v[242:245], v[16:19]
	v_cvt_pk_bf16_f32 v238, v68, v69
	v_mfma_f32_16x16x32_bf16 v[20:23], v[180:183], v[204:207], v[20:23]
	v_cvt_pk_bf16_f32 v239, v70, v71
	ds_read_b128 v[176:179], v203 offset:28672
	s_waitcnt lgkmcnt(6)
	v_mfma_f32_16x16x32_bf16 v[84:87], v[230:233], v[124:127], v[84:87]
	v_cvt_pk_bf16_f32 v218, v72, v73
	v_mfma_f32_16x16x32_bf16 v[80:83], v[230:233], v[108:111], v[80:83]
	v_cvt_pk_bf16_f32 v219, v74, v75
	ds_read_b128 v[180:183], v210 offset:12288
	s_waitcnt lgkmcnt(6)
	v_mfma_f32_16x16x32_bf16 v[28:31], v[234:237], v[204:207], v[28:31]
	v_cvt_pk_bf16_f32 v240, v76, v77
	v_mfma_f32_16x16x32_bf16 v[24:27], v[234:237], v[242:245], v[24:27]
	v_cvt_pk_bf16_f32 v241, v78, v79
	ds_read_b128 v[230:233], v246 offset:28672
	s_waitcnt lgkmcnt(6)
	v_mfma_f32_16x16x32_bf16 v[88:91], v[160:163], v[96:99], 0
	v_exp_f32_e32 v80, v80
	v_mfma_f32_16x16x32_bf16 v[92:95], v[160:163], v[112:115], 0
	v_exp_f32_e32 v84, v84
	ds_read_b128 v[234:237], v210 offset:14336
	s_waitcnt lgkmcnt(6)
	v_mfma_f32_16x16x32_bf16 v[32:35], v[164:167], v[242:245], v[32:35]
	v_exp_f32_e32 v81, v81
	v_mfma_f32_16x16x32_bf16 v[36:39], v[164:167], v[204:207], v[36:39]
	v_exp_f32_e32 v85, v85
	ds_read_b128 v[160:163], v201 offset:32768
	s_waitcnt lgkmcnt(6)
	v_mfma_f32_16x16x32_bf16 v[92:95], v[168:171], v[116:119], v[92:95]
	v_exp_f32_e32 v82, v82
	v_mfma_f32_16x16x32_bf16 v[88:91], v[168:171], v[100:103], v[88:91]
	v_exp_f32_e32 v86, v86
	ds_read_b128 v[164:167], v209 offset:16384
	s_waitcnt lgkmcnt(6)
	v_mfma_f32_16x16x32_bf16 v[44:47], v[172:175], v[204:207], v[44:47]
	v_exp_f32_e32 v83, v83
	v_mfma_f32_16x16x32_bf16 v[40:43], v[172:175], v[242:245], v[40:43]
	v_exp_f32_e32 v87, v87
	ds_read_b128 v[168:171], v202 offset:32768
	s_waitcnt lgkmcnt(6)
	v_mfma_f32_16x16x32_bf16 v[88:91], v[176:179], v[104:107], v[88:91]
	v_add_f32_e32 v220, v220, v80
	v_mfma_f32_16x16x32_bf16 v[92:95], v[176:179], v[120:123], v[92:95]
	v_add_f32_e32 v221, v221, v84
	ds_read_b128 v[172:175], v209 offset:18432
	s_waitcnt lgkmcnt(6)
	v_mfma_f32_16x16x32_bf16 v[48:51], v[180:183], v[242:245], v[48:51]
	v_add_f32_e32 v220, v220, v81
	v_mfma_f32_16x16x32_bf16 v[52:55], v[180:183], v[204:207], v[52:55]
	v_add_f32_e32 v221, v221, v85
	ds_read_b128 v[176:179], v203 offset:32768
	s_waitcnt lgkmcnt(6)
	v_mfma_f32_16x16x32_bf16 v[92:95], v[230:233], v[124:127], v[92:95]
	v_add_f32_e32 v220, v220, v82
	v_mfma_f32_16x16x32_bf16 v[88:91], v[230:233], v[108:111], v[88:91]
	v_add_f32_e32 v221, v221, v86
	ds_read_b128 v[180:183], v209 offset:20480
	s_waitcnt lgkmcnt(6)
	v_mfma_f32_16x16x32_bf16 v[60:63], v[234:237], v[204:207], v[60:63]
	v_add_f32_e32 v220, v220, v83
	v_mfma_f32_16x16x32_bf16 v[56:59], v[234:237], v[242:245], v[56:59]
	v_add_f32_e32 v221, v221, v87
	ds_read_b128 v[230:233], v246 offset:32768
	s_waitcnt lgkmcnt(6)
	v_mfma_f32_16x16x32_bf16 v[64:67], v[160:163], v[96:99], 0
	v_exp_f32_e32 v88, v88
	v_exp_f32_e32 v92, v92
	v_mfma_f32_16x16x32_bf16 v[68:71], v[160:163], v[112:115], 0
	v_exp_f32_e32 v89, v89
	v_exp_f32_e32 v93, v93
	ds_read_b128 v[234:237], v209 offset:22528
	s_add_u32 s8, s16, 0x3bc00280
	s_addc_u32 s9, s17, 0
	s_add_u32 s6, s15, 0x23a60000
	s_addc_u32 s7, s14, 0
	s_waitcnt lgkmcnt(6)
	v_mfma_f32_16x16x32_bf16 v[0:3], v[164:167], v[216:219], v[0:3]
	v_exp_f32_e32 v90, v90
	v_exp_f32_e32 v94, v94
	v_mfma_f32_16x16x32_bf16 v[4:7], v[164:167], v[238:241], v[4:7]
	v_exp_f32_e32 v91, v91
	v_exp_f32_e32 v95, v95
	ds_read_b128 v[160:163], v201 offset:36864
	s_waitcnt vmcnt(4)
	ds_write_b128 v225, v[136:139] offset:0
	s_waitcnt lgkmcnt(7)
	v_mfma_f32_16x16x32_bf16 v[68:71], v[168:171], v[116:119], v[68:71]
	v_add_f32_e32 v220, v220, v88
	v_add_f32_e32 v221, v221, v92
	v_mfma_f32_16x16x32_bf16 v[64:67], v[168:171], v[100:103], v[64:67]
	v_add_f32_e32 v220, v220, v89
	v_add_f32_e32 v221, v221, v93
	ds_read_b128 v[164:167], v209 offset:24576
	ds_write_b128 v226, v[140:143] offset:0
	s_waitcnt lgkmcnt(8)
	v_mfma_f32_16x16x32_bf16 v[12:15], v[172:175], v[238:241], v[12:15]
	v_add_f32_e32 v220, v220, v90
	v_add_f32_e32 v221, v221, v94
	v_mfma_f32_16x16x32_bf16 v[8:11], v[172:175], v[216:219], v[8:11]
	v_add_f32_e32 v220, v220, v91
	v_add_f32_e32 v221, v221, v95
	ds_read_b128 v[168:171], v202 offset:36864
	ds_write_b64 v227, v[148:149] offset:49152
	s_waitcnt lgkmcnt(9)
	v_mfma_f32_16x16x32_bf16 v[64:67], v[176:179], v[104:107], v[64:67]
	v_add_f32_e32 v194, v194, v220
	v_add_f32_e32 v195, v195, v221
	v_mfma_f32_16x16x32_bf16 v[68:71], v[176:179], v[120:123], v[68:71]
	v_cvt_pk_bf16_f32 v242, v80, v81
	v_cvt_pk_bf16_f32 v243, v82, v83
	ds_read_b128 v[172:175], v209 offset:26624
	ds_write_b64 v228, v[150:151] offset:49152
	s_waitcnt lgkmcnt(10)
	v_mfma_f32_16x16x32_bf16 v[16:19], v[180:183], v[216:219], v[16:19]
	v_cvt_pk_bf16_f32 v204, v84, v85
	v_mfma_f32_16x16x32_bf16 v[20:23], v[180:183], v[238:241], v[20:23]
	v_cvt_pk_bf16_f32 v205, v86, v87
	ds_read_b128 v[176:179], v203 offset:36864
	ds_write_b64 v229, v[144:145] offset:49152
	s_waitcnt lgkmcnt(11)
	v_mfma_f32_16x16x32_bf16 v[68:71], v[230:233], v[124:127], v[68:71]
	v_cvt_pk_bf16_f32 v244, v88, v89
	v_mfma_f32_16x16x32_bf16 v[64:67], v[230:233], v[108:111], v[64:67]
	v_cvt_pk_bf16_f32 v245, v90, v91
	ds_read_b128 v[180:183], v209 offset:28672
	ds_write_b64 v184, v[146:147] offset:49152
	s_waitcnt lgkmcnt(12)
	v_mfma_f32_16x16x32_bf16 v[28:31], v[234:237], v[238:241], v[28:31]
	v_cvt_pk_bf16_f32 v206, v92, v93
	v_mfma_f32_16x16x32_bf16 v[24:27], v[234:237], v[216:219], v[24:27]
	v_cvt_pk_bf16_f32 v207, v94, v95
	ds_read_b128 v[230:233], v246 offset:36864
	global_load_dwordx4 v[148:151], v198, s[8:9]
	s_waitcnt lgkmcnt(12)
	v_mfma_f32_16x16x32_bf16 v[72:75], v[160:163], v[96:99], 0
	v_exp_f32_e32 v64, v64
	v_mfma_f32_16x16x32_bf16 v[76:79], v[160:163], v[112:115], 0
	v_exp_f32_e32 v68, v68
	ds_read_b128 v[234:237], v209 offset:30720
	global_load_dwordx4 v[144:147], v199, s[8:9]
	s_waitcnt lgkmcnt(11)
	v_mfma_f32_16x16x32_bf16 v[32:35], v[164:167], v[216:219], v[32:35]
	v_exp_f32_e32 v65, v65
	v_mfma_f32_16x16x32_bf16 v[36:39], v[164:167], v[238:241], v[36:39]
	v_exp_f32_e32 v69, v69
	ds_read_b128 v[160:163], v201 offset:40960
	global_load_dwordx4 v[136:139], v196, s[6:7]
	s_waitcnt lgkmcnt(10)
	v_mfma_f32_16x16x32_bf16 v[76:79], v[168:171], v[116:119], v[76:79]
	v_exp_f32_e32 v66, v66
	v_mfma_f32_16x16x32_bf16 v[72:75], v[168:171], v[100:103], v[72:75]
	v_exp_f32_e32 v70, v70
	ds_read_b128 v[164:167], v210 offset:16384
	global_load_dwordx4 v[140:143], v197, s[6:7]
	s_waitcnt lgkmcnt(9)
	v_mfma_f32_16x16x32_bf16 v[44:47], v[172:175], v[238:241], v[44:47]
	v_exp_f32_e32 v67, v67
	v_mfma_f32_16x16x32_bf16 v[40:43], v[172:175], v[216:219], v[40:43]
	v_exp_f32_e32 v71, v71
	ds_read_b128 v[168:171], v202 offset:40960
	s_waitcnt lgkmcnt(8)
	v_mfma_f32_16x16x32_bf16 v[72:75], v[176:179], v[104:107], v[72:75]
	v_add_f32_e32 v220, v64, v65
	v_mfma_f32_16x16x32_bf16 v[76:79], v[176:179], v[120:123], v[76:79]
	v_add_f32_e32 v221, v68, v69
	ds_read_b128 v[172:175], v210 offset:18432
	s_waitcnt lgkmcnt(7)
	v_mfma_f32_16x16x32_bf16 v[48:51], v[180:183], v[216:219], v[48:51]
	v_add_f32_e32 v220, v220, v66
	v_mfma_f32_16x16x32_bf16 v[52:55], v[180:183], v[238:241], v[52:55]
	v_add_f32_e32 v221, v221, v70
	ds_read_b128 v[176:179], v203 offset:40960
	s_waitcnt lgkmcnt(6)
	v_mfma_f32_16x16x32_bf16 v[76:79], v[230:233], v[124:127], v[76:79]
	v_add_f32_e32 v220, v220, v67
	v_mfma_f32_16x16x32_bf16 v[72:75], v[230:233], v[108:111], v[72:75]
	v_add_f32_e32 v221, v221, v71
	ds_read_b128 v[180:183], v210 offset:20480
	s_waitcnt lgkmcnt(6)
	v_mfma_f32_16x16x32_bf16 v[60:63], v[234:237], v[238:241], v[60:63]
	v_mfma_f32_16x16x32_bf16 v[56:59], v[234:237], v[216:219], v[56:59]
	ds_read_b128 v[230:233], v246 offset:40960
	s_waitcnt lgkmcnt(6)
	v_mfma_f32_16x16x32_bf16 v[80:83], v[160:163], v[96:99], 0
	v_exp_f32_e32 v72, v72
	v_exp_f32_e32 v76, v76
	v_mfma_f32_16x16x32_bf16 v[84:87], v[160:163], v[112:115], 0
	v_exp_f32_e32 v73, v73
	v_exp_f32_e32 v77, v77
	ds_read_b128 v[234:237], v210 offset:22528
	s_waitcnt lgkmcnt(6)
	v_mfma_f32_16x16x32_bf16 v[0:3], v[164:167], v[242:245], v[0:3]
	v_exp_f32_e32 v74, v74
	v_exp_f32_e32 v78, v78
	v_mfma_f32_16x16x32_bf16 v[4:7], v[164:167], v[204:207], v[4:7]
	v_exp_f32_e32 v75, v75
	v_exp_f32_e32 v79, v79
	ds_read_b128 v[160:163], v201 offset:45056
	s_waitcnt lgkmcnt(6)
	v_mfma_f32_16x16x32_bf16 v[84:87], v[168:171], v[116:119], v[84:87]
	v_add_f32_e32 v220, v220, v72
	v_add_f32_e32 v221, v221, v76
	v_mfma_f32_16x16x32_bf16 v[80:83], v[168:171], v[100:103], v[80:83]
	v_add_f32_e32 v220, v220, v73
	v_add_f32_e32 v221, v221, v77
	ds_read_b128 v[164:167], v210 offset:24576
	s_waitcnt lgkmcnt(6)
	v_mfma_f32_16x16x32_bf16 v[12:15], v[172:175], v[204:207], v[12:15]
	v_add_f32_e32 v220, v220, v74
	v_add_f32_e32 v221, v221, v78
	v_mfma_f32_16x16x32_bf16 v[8:11], v[172:175], v[242:245], v[8:11]
	v_add_f32_e32 v220, v220, v75
	v_add_f32_e32 v221, v221, v79
	ds_read_b128 v[168:171], v202 offset:45056
	s_waitcnt lgkmcnt(6)
	v_mfma_f32_16x16x32_bf16 v[80:83], v[176:179], v[104:107], v[80:83]
	v_cvt_pk_bf16_f32 v216, v64, v65
	v_mfma_f32_16x16x32_bf16 v[84:87], v[176:179], v[120:123], v[84:87]
	v_cvt_pk_bf16_f32 v217, v66, v67
	ds_read_b128 v[172:175], v210 offset:26624
	s_waitcnt lgkmcnt(6)
	v_mfma_f32_16x16x32_bf16 v[16:19], v[180:183], v[242:245], v[16:19]
	v_cvt_pk_bf16_f32 v238, v68, v69
	v_mfma_f32_16x16x32_bf16 v[20:23], v[180:183], v[204:207], v[20:23]
	v_cvt_pk_bf16_f32 v239, v70, v71
	ds_read_b128 v[176:179], v203 offset:45056
	s_waitcnt lgkmcnt(6)
	v_mfma_f32_16x16x32_bf16 v[84:87], v[230:233], v[124:127], v[84:87]
	v_cvt_pk_bf16_f32 v218, v72, v73
	v_mfma_f32_16x16x32_bf16 v[80:83], v[230:233], v[108:111], v[80:83]
	v_cvt_pk_bf16_f32 v219, v74, v75
	ds_read_b128 v[180:183], v210 offset:28672
	s_waitcnt lgkmcnt(6)
	v_mfma_f32_16x16x32_bf16 v[28:31], v[234:237], v[204:207], v[28:31]
	v_cvt_pk_bf16_f32 v240, v76, v77
	v_mfma_f32_16x16x32_bf16 v[24:27], v[234:237], v[242:245], v[24:27]
	v_cvt_pk_bf16_f32 v241, v78, v79
	ds_read_b128 v[230:233], v246 offset:45056
	s_waitcnt lgkmcnt(6)
	v_mfma_f32_16x16x32_bf16 v[88:91], v[160:163], v[96:99], 0
	v_exp_f32_e32 v80, v80
	v_mfma_f32_16x16x32_bf16 v[92:95], v[160:163], v[112:115], 0
	v_exp_f32_e32 v84, v84
	ds_read_b128 v[234:237], v210 offset:30720
	s_waitcnt lgkmcnt(6)
	v_mfma_f32_16x16x32_bf16 v[32:35], v[164:167], v[242:245], v[32:35]
	v_exp_f32_e32 v81, v81
	v_mfma_f32_16x16x32_bf16 v[36:39], v[164:167], v[204:207], v[36:39]
	v_exp_f32_e32 v85, v85
	s_waitcnt lgkmcnt(5)
	v_mfma_f32_16x16x32_bf16 v[92:95], v[168:171], v[116:119], v[92:95]
	v_exp_f32_e32 v82, v82
	v_mfma_f32_16x16x32_bf16 v[88:91], v[168:171], v[100:103], v[88:91]
	v_exp_f32_e32 v86, v86
	s_waitcnt lgkmcnt(4)
	v_mfma_f32_16x16x32_bf16 v[44:47], v[172:175], v[204:207], v[44:47]
	v_exp_f32_e32 v83, v83
	v_mfma_f32_16x16x32_bf16 v[40:43], v[172:175], v[242:245], v[40:43]
	v_exp_f32_e32 v87, v87
	s_waitcnt lgkmcnt(3)
	v_mfma_f32_16x16x32_bf16 v[88:91], v[176:179], v[104:107], v[88:91]
	v_add_f32_e32 v220, v220, v80
	v_mfma_f32_16x16x32_bf16 v[92:95], v[176:179], v[120:123], v[92:95]
	v_add_f32_e32 v221, v221, v84
	s_waitcnt lgkmcnt(2)
	v_mfma_f32_16x16x32_bf16 v[48:51], v[180:183], v[242:245], v[48:51]
	v_add_f32_e32 v220, v220, v81
	v_mfma_f32_16x16x32_bf16 v[52:55], v[180:183], v[204:207], v[52:55]
	v_add_f32_e32 v221, v221, v85
	s_waitcnt lgkmcnt(1)
	v_mfma_f32_16x16x32_bf16 v[92:95], v[230:233], v[124:127], v[92:95]
	v_add_f32_e32 v220, v220, v82
	v_mfma_f32_16x16x32_bf16 v[88:91], v[230:233], v[108:111], v[88:91]
	v_add_f32_e32 v221, v221, v86
	s_waitcnt lgkmcnt(0)
	v_mfma_f32_16x16x32_bf16 v[60:63], v[234:237], v[204:207], v[60:63]
	v_add_f32_e32 v220, v220, v83
	v_mfma_f32_16x16x32_bf16 v[56:59], v[234:237], v[242:245], v[56:59]
	v_add_f32_e32 v221, v221, v87
	s_waitcnt lgkmcnt(0)
	s_barrier
	ds_read_b128 v[160:163], v201 offset:49152
	ds_read_b128 v[164:167], v209 offset:32768
	ds_read_b128 v[168:171], v202 offset:49152
	ds_read_b128 v[172:175], v209 offset:34816
	ds_read_b128 v[176:179], v203 offset:49152
	ds_read_b128 v[180:183], v209 offset:36864
	ds_read_b128 v[230:233], v246 offset:49152
	s_waitcnt lgkmcnt(6)
	v_mfma_f32_16x16x32_bf16 v[64:67], v[160:163], v[96:99], 0
	v_exp_f32_e32 v88, v88
	v_exp_f32_e32 v92, v92
	v_mfma_f32_16x16x32_bf16 v[68:71], v[160:163], v[112:115], 0
	v_exp_f32_e32 v89, v89
	v_exp_f32_e32 v93, v93
	ds_read_b128 v[234:237], v209 offset:38912
	s_add_u32 s8, s16, 0x3bc00300
	s_addc_u32 s9, s17, 0
	s_add_u32 s6, s15, 0x23a70000
	s_addc_u32 s7, s14, 0
	s_waitcnt lgkmcnt(6)
	v_mfma_f32_16x16x32_bf16 v[0:3], v[164:167], v[216:219], v[0:3]
	v_exp_f32_e32 v90, v90
	v_exp_f32_e32 v94, v94
	v_mfma_f32_16x16x32_bf16 v[4:7], v[164:167], v[238:241], v[4:7]
	v_exp_f32_e32 v91, v91
	v_exp_f32_e32 v95, v95
	ds_read_b128 v[160:163], v201 offset:53248
	s_waitcnt vmcnt(4)
	ds_write_b128 v225, v[152:155] offset:16384
	s_waitcnt lgkmcnt(7)
	v_mfma_f32_16x16x32_bf16 v[68:71], v[168:171], v[116:119], v[68:71]
	v_add_f32_e32 v220, v220, v88
	v_add_f32_e32 v221, v221, v92
	v_mfma_f32_16x16x32_bf16 v[64:67], v[168:171], v[100:103], v[64:67]
	v_add_f32_e32 v220, v220, v89
	v_add_f32_e32 v221, v221, v93
	ds_read_b128 v[164:167], v209 offset:40960
	ds_write_b128 v226, v[156:159] offset:16384
	s_waitcnt lgkmcnt(8)
	v_mfma_f32_16x16x32_bf16 v[12:15], v[172:175], v[238:241], v[12:15]
	v_add_f32_e32 v220, v220, v90
	v_add_f32_e32 v221, v221, v94
	v_mfma_f32_16x16x32_bf16 v[8:11], v[172:175], v[216:219], v[8:11]
	v_add_f32_e32 v220, v220, v91
	v_add_f32_e32 v221, v221, v95
	ds_read_b128 v[168:171], v202 offset:53248
	ds_write_b64 v227, v[132:133] offset:0
	s_waitcnt lgkmcnt(9)
	v_mfma_f32_16x16x32_bf16 v[64:67], v[176:179], v[104:107], v[64:67]
	v_add_f32_e32 v194, v194, v220
	v_add_f32_e32 v195, v195, v221
	v_mfma_f32_16x16x32_bf16 v[68:71], v[176:179], v[120:123], v[68:71]
	v_cvt_pk_bf16_f32 v242, v80, v81
	v_cvt_pk_bf16_f32 v243, v82, v83
	ds_read_b128 v[172:175], v209 offset:43008
	ds_write_b64 v228, v[134:135] offset:0
	s_waitcnt lgkmcnt(10)
	v_mfma_f32_16x16x32_bf16 v[16:19], v[180:183], v[216:219], v[16:19]
	v_cvt_pk_bf16_f32 v204, v84, v85
	v_mfma_f32_16x16x32_bf16 v[20:23], v[180:183], v[238:241], v[20:23]
	v_cvt_pk_bf16_f32 v205, v86, v87
	ds_read_b128 v[176:179], v203 offset:53248
	ds_write_b64 v229, v[128:129] offset:0
	s_waitcnt lgkmcnt(11)
	v_mfma_f32_16x16x32_bf16 v[68:71], v[230:233], v[124:127], v[68:71]
	v_cvt_pk_bf16_f32 v244, v88, v89
	v_mfma_f32_16x16x32_bf16 v[64:67], v[230:233], v[108:111], v[64:67]
	v_cvt_pk_bf16_f32 v245, v90, v91
	ds_read_b128 v[180:183], v209 offset:45056
	ds_write_b64 v184, v[130:131] offset:0
	s_waitcnt lgkmcnt(12)
	v_mfma_f32_16x16x32_bf16 v[28:31], v[234:237], v[238:241], v[28:31]
	v_cvt_pk_bf16_f32 v206, v92, v93
	v_mfma_f32_16x16x32_bf16 v[24:27], v[234:237], v[216:219], v[24:27]
	v_cvt_pk_bf16_f32 v207, v94, v95
	ds_read_b128 v[230:233], v246 offset:53248
	global_load_dwordx4 v[132:135], v198, s[8:9]
	s_waitcnt lgkmcnt(12)
	v_mfma_f32_16x16x32_bf16 v[72:75], v[160:163], v[96:99], 0
	v_exp_f32_e32 v64, v64
	v_mfma_f32_16x16x32_bf16 v[76:79], v[160:163], v[112:115], 0
	v_exp_f32_e32 v68, v68
	ds_read_b128 v[234:237], v209 offset:47104
	global_load_dwordx4 v[128:131], v199, s[8:9]
	s_waitcnt lgkmcnt(11)
	v_mfma_f32_16x16x32_bf16 v[32:35], v[164:167], v[216:219], v[32:35]
	v_exp_f32_e32 v65, v65
	v_mfma_f32_16x16x32_bf16 v[36:39], v[164:167], v[238:241], v[36:39]
	v_exp_f32_e32 v69, v69
	ds_read_b128 v[160:163], v201 offset:57344
	global_load_dwordx4 v[152:155], v196, s[6:7]
	s_waitcnt lgkmcnt(10)
	v_mfma_f32_16x16x32_bf16 v[76:79], v[168:171], v[116:119], v[76:79]
	v_exp_f32_e32 v66, v66
	v_mfma_f32_16x16x32_bf16 v[72:75], v[168:171], v[100:103], v[72:75]
	v_exp_f32_e32 v70, v70
	ds_read_b128 v[164:167], v210 offset:32768
	global_load_dwordx4 v[156:159], v197, s[6:7]
	s_waitcnt lgkmcnt(9)
	v_mfma_f32_16x16x32_bf16 v[44:47], v[172:175], v[238:241], v[44:47]
	v_exp_f32_e32 v67, v67
	v_mfma_f32_16x16x32_bf16 v[40:43], v[172:175], v[216:219], v[40:43]
	v_exp_f32_e32 v71, v71
	ds_read_b128 v[168:171], v202 offset:57344
	s_waitcnt lgkmcnt(8)
	v_mfma_f32_16x16x32_bf16 v[72:75], v[176:179], v[104:107], v[72:75]
	v_add_f32_e32 v220, v64, v65
	v_mfma_f32_16x16x32_bf16 v[76:79], v[176:179], v[120:123], v[76:79]
	v_add_f32_e32 v221, v68, v69
	ds_read_b128 v[172:175], v210 offset:34816
	s_waitcnt lgkmcnt(7)
	v_mfma_f32_16x16x32_bf16 v[48:51], v[180:183], v[216:219], v[48:51]
	v_add_f32_e32 v220, v220, v66
	v_mfma_f32_16x16x32_bf16 v[52:55], v[180:183], v[238:241], v[52:55]
	v_add_f32_e32 v221, v221, v70
	ds_read_b128 v[176:179], v203 offset:57344
	s_waitcnt lgkmcnt(6)
	v_mfma_f32_16x16x32_bf16 v[76:79], v[230:233], v[124:127], v[76:79]
	v_add_f32_e32 v220, v220, v67
	v_mfma_f32_16x16x32_bf16 v[72:75], v[230:233], v[108:111], v[72:75]
	v_add_f32_e32 v221, v221, v71
	ds_read_b128 v[180:183], v210 offset:36864
	s_waitcnt lgkmcnt(6)
	v_mfma_f32_16x16x32_bf16 v[60:63], v[234:237], v[238:241], v[60:63]
	v_mfma_f32_16x16x32_bf16 v[56:59], v[234:237], v[216:219], v[56:59]
	ds_read_b128 v[230:233], v246 offset:57344
	s_waitcnt lgkmcnt(6)
	v_mfma_f32_16x16x32_bf16 v[80:83], v[160:163], v[96:99], 0
	v_exp_f32_e32 v72, v72
	v_exp_f32_e32 v76, v76
	v_mfma_f32_16x16x32_bf16 v[84:87], v[160:163], v[112:115], 0
	v_exp_f32_e32 v73, v73
	v_exp_f32_e32 v77, v77
	ds_read_b128 v[234:237], v210 offset:38912
	s_waitcnt lgkmcnt(6)
	v_mfma_f32_16x16x32_bf16 v[0:3], v[164:167], v[242:245], v[0:3]
	v_exp_f32_e32 v74, v74
	v_exp_f32_e32 v78, v78
	v_mfma_f32_16x16x32_bf16 v[4:7], v[164:167], v[204:207], v[4:7]
	v_exp_f32_e32 v75, v75
	v_exp_f32_e32 v79, v79
	ds_read_b128 v[160:163], v201 offset:61440
	s_waitcnt lgkmcnt(6)
	v_mfma_f32_16x16x32_bf16 v[84:87], v[168:171], v[116:119], v[84:87]
	v_add_f32_e32 v220, v220, v72
	v_add_f32_e32 v221, v221, v76
	v_mfma_f32_16x16x32_bf16 v[80:83], v[168:171], v[100:103], v[80:83]
	v_add_f32_e32 v220, v220, v73
	v_add_f32_e32 v221, v221, v77
	ds_read_b128 v[164:167], v210 offset:40960
	s_waitcnt lgkmcnt(6)
	v_mfma_f32_16x16x32_bf16 v[12:15], v[172:175], v[204:207], v[12:15]
	v_add_f32_e32 v220, v220, v74
	v_add_f32_e32 v221, v221, v78
	v_mfma_f32_16x16x32_bf16 v[8:11], v[172:175], v[242:245], v[8:11]
	v_add_f32_e32 v220, v220, v75
	v_add_f32_e32 v221, v221, v79
	ds_read_b128 v[168:171], v202 offset:61440
	s_waitcnt lgkmcnt(6)
	v_mfma_f32_16x16x32_bf16 v[80:83], v[176:179], v[104:107], v[80:83]
	v_cvt_pk_bf16_f32 v216, v64, v65
	v_mfma_f32_16x16x32_bf16 v[84:87], v[176:179], v[120:123], v[84:87]
	v_cvt_pk_bf16_f32 v217, v66, v67
	ds_read_b128 v[172:175], v210 offset:43008
	s_waitcnt lgkmcnt(6)
	v_mfma_f32_16x16x32_bf16 v[16:19], v[180:183], v[242:245], v[16:19]
	v_cvt_pk_bf16_f32 v238, v68, v69
	v_mfma_f32_16x16x32_bf16 v[20:23], v[180:183], v[204:207], v[20:23]
	v_cvt_pk_bf16_f32 v239, v70, v71
	ds_read_b128 v[176:179], v203 offset:61440
	s_waitcnt lgkmcnt(6)
	v_mfma_f32_16x16x32_bf16 v[84:87], v[230:233], v[124:127], v[84:87]
	v_cvt_pk_bf16_f32 v218, v72, v73
	v_mfma_f32_16x16x32_bf16 v[80:83], v[230:233], v[108:111], v[80:83]
	v_cvt_pk_bf16_f32 v219, v74, v75
	ds_read_b128 v[180:183], v210 offset:45056
	s_waitcnt lgkmcnt(6)
	v_mfma_f32_16x16x32_bf16 v[28:31], v[234:237], v[204:207], v[28:31]
	v_cvt_pk_bf16_f32 v240, v76, v77
	v_mfma_f32_16x16x32_bf16 v[24:27], v[234:237], v[242:245], v[24:27]
	v_cvt_pk_bf16_f32 v241, v78, v79
	ds_read_b128 v[230:233], v246 offset:61440
	s_waitcnt lgkmcnt(6)
	v_mfma_f32_16x16x32_bf16 v[88:91], v[160:163], v[96:99], 0
	v_exp_f32_e32 v80, v80
	v_mfma_f32_16x16x32_bf16 v[92:95], v[160:163], v[112:115], 0
	v_exp_f32_e32 v84, v84
	ds_read_b128 v[234:237], v210 offset:47104
	s_waitcnt lgkmcnt(6)
	v_mfma_f32_16x16x32_bf16 v[32:35], v[164:167], v[242:245], v[32:35]
	v_exp_f32_e32 v81, v81
	v_mfma_f32_16x16x32_bf16 v[36:39], v[164:167], v[204:207], v[36:39]
	v_exp_f32_e32 v85, v85
	ds_read_b128 v[160:163], v201 offset:0
	s_waitcnt lgkmcnt(6)
	v_mfma_f32_16x16x32_bf16 v[92:95], v[168:171], v[116:119], v[92:95]
	v_exp_f32_e32 v82, v82
	v_mfma_f32_16x16x32_bf16 v[88:91], v[168:171], v[100:103], v[88:91]
	v_exp_f32_e32 v86, v86
	ds_read_b128 v[164:167], v209 offset:49152
	s_waitcnt lgkmcnt(6)
	v_mfma_f32_16x16x32_bf16 v[44:47], v[172:175], v[204:207], v[44:47]
	v_exp_f32_e32 v83, v83
	v_mfma_f32_16x16x32_bf16 v[40:43], v[172:175], v[242:245], v[40:43]
	v_exp_f32_e32 v87, v87
	ds_read_b128 v[168:171], v202 offset:0
	s_waitcnt lgkmcnt(6)
	v_mfma_f32_16x16x32_bf16 v[88:91], v[176:179], v[104:107], v[88:91]
	v_add_f32_e32 v220, v220, v80
	v_mfma_f32_16x16x32_bf16 v[92:95], v[176:179], v[120:123], v[92:95]
	v_add_f32_e32 v221, v221, v84
	ds_read_b128 v[172:175], v209 offset:51200
	s_waitcnt lgkmcnt(6)
	v_mfma_f32_16x16x32_bf16 v[48:51], v[180:183], v[242:245], v[48:51]
	v_add_f32_e32 v220, v220, v81
	v_mfma_f32_16x16x32_bf16 v[52:55], v[180:183], v[204:207], v[52:55]
	v_add_f32_e32 v221, v221, v85
	ds_read_b128 v[176:179], v203 offset:0
	s_waitcnt lgkmcnt(6)
	v_mfma_f32_16x16x32_bf16 v[92:95], v[230:233], v[124:127], v[92:95]
	v_add_f32_e32 v220, v220, v82
	v_mfma_f32_16x16x32_bf16 v[88:91], v[230:233], v[108:111], v[88:91]
	v_add_f32_e32 v221, v221, v86
	ds_read_b128 v[180:183], v209 offset:53248
	s_waitcnt lgkmcnt(6)
	v_mfma_f32_16x16x32_bf16 v[60:63], v[234:237], v[204:207], v[60:63]
	v_add_f32_e32 v220, v220, v83
	v_mfma_f32_16x16x32_bf16 v[56:59], v[234:237], v[242:245], v[56:59]
	v_add_f32_e32 v221, v221, v87
	ds_read_b128 v[230:233], v246 offset:0
	s_waitcnt lgkmcnt(6)
	v_mfma_f32_16x16x32_bf16 v[64:67], v[160:163], v[96:99], 0
	v_exp_f32_e32 v88, v88
	v_exp_f32_e32 v92, v92
	v_mfma_f32_16x16x32_bf16 v[68:71], v[160:163], v[112:115], 0
	v_exp_f32_e32 v89, v89
	v_exp_f32_e32 v93, v93
	ds_read_b128 v[234:237], v209 offset:55296
	s_add_u32 s8, s16, 0x3bc00380
	s_addc_u32 s9, s17, 0
	s_add_u32 s6, s15, 0x23a80000
	s_addc_u32 s7, s14, 0
	s_waitcnt lgkmcnt(6)
	v_mfma_f32_16x16x32_bf16 v[0:3], v[164:167], v[216:219], v[0:3]
	v_exp_f32_e32 v90, v90
	v_exp_f32_e32 v94, v94
	v_mfma_f32_16x16x32_bf16 v[4:7], v[164:167], v[238:241], v[4:7]
	v_exp_f32_e32 v91, v91
	v_exp_f32_e32 v95, v95
	ds_read_b128 v[160:163], v201 offset:4096
	s_waitcnt vmcnt(4)
	ds_write_b128 v225, v[136:139] offset:32768
	s_waitcnt lgkmcnt(7)
	v_mfma_f32_16x16x32_bf16 v[68:71], v[168:171], v[116:119], v[68:71]
	v_add_f32_e32 v220, v220, v88
	v_add_f32_e32 v221, v221, v92
	v_mfma_f32_16x16x32_bf16 v[64:67], v[168:171], v[100:103], v[64:67]
	v_add_f32_e32 v220, v220, v89
	v_add_f32_e32 v221, v221, v93
	ds_read_b128 v[164:167], v209 offset:57344
	ds_write_b128 v226, v[140:143] offset:32768
	s_waitcnt lgkmcnt(8)
	v_mfma_f32_16x16x32_bf16 v[12:15], v[172:175], v[238:241], v[12:15]
	v_add_f32_e32 v220, v220, v90
	v_add_f32_e32 v221, v221, v94
	v_mfma_f32_16x16x32_bf16 v[8:11], v[172:175], v[216:219], v[8:11]
	v_add_f32_e32 v220, v220, v91
	v_add_f32_e32 v221, v221, v95
	ds_read_b128 v[168:171], v202 offset:4096
	ds_write_b64 v227, v[148:149] offset:16384
	s_waitcnt lgkmcnt(9)
	v_mfma_f32_16x16x32_bf16 v[64:67], v[176:179], v[104:107], v[64:67]
	v_add_f32_e32 v194, v194, v220
	v_add_f32_e32 v195, v195, v221
	v_mfma_f32_16x16x32_bf16 v[68:71], v[176:179], v[120:123], v[68:71]
	v_cvt_pk_bf16_f32 v242, v80, v81
	v_cvt_pk_bf16_f32 v243, v82, v83
	ds_read_b128 v[172:175], v209 offset:59392
	ds_write_b64 v228, v[150:151] offset:16384
	s_waitcnt lgkmcnt(10)
	v_mfma_f32_16x16x32_bf16 v[16:19], v[180:183], v[216:219], v[16:19]
	v_cvt_pk_bf16_f32 v204, v84, v85
	v_mfma_f32_16x16x32_bf16 v[20:23], v[180:183], v[238:241], v[20:23]
	v_cvt_pk_bf16_f32 v205, v86, v87
	ds_read_b128 v[176:179], v203 offset:4096
	ds_write_b64 v229, v[144:145] offset:16384
	s_waitcnt lgkmcnt(11)
	v_mfma_f32_16x16x32_bf16 v[68:71], v[230:233], v[124:127], v[68:71]
	v_cvt_pk_bf16_f32 v244, v88, v89
	v_mfma_f32_16x16x32_bf16 v[64:67], v[230:233], v[108:111], v[64:67]
	v_cvt_pk_bf16_f32 v245, v90, v91
	ds_read_b128 v[180:183], v209 offset:61440
	ds_write_b64 v184, v[146:147] offset:16384
	s_waitcnt lgkmcnt(12)
	v_mfma_f32_16x16x32_bf16 v[28:31], v[234:237], v[238:241], v[28:31]
	v_cvt_pk_bf16_f32 v206, v92, v93
	v_mfma_f32_16x16x32_bf16 v[24:27], v[234:237], v[216:219], v[24:27]
	v_cvt_pk_bf16_f32 v207, v94, v95
	ds_read_b128 v[230:233], v246 offset:4096
	global_load_dwordx4 v[148:151], v198, s[8:9]
	s_waitcnt lgkmcnt(12)
	v_mfma_f32_16x16x32_bf16 v[72:75], v[160:163], v[96:99], 0
	v_exp_f32_e32 v64, v64
	v_mfma_f32_16x16x32_bf16 v[76:79], v[160:163], v[112:115], 0
	v_exp_f32_e32 v68, v68
	ds_read_b128 v[234:237], v209 offset:63488
	global_load_dwordx4 v[144:147], v199, s[8:9]
	s_waitcnt lgkmcnt(11)
	v_mfma_f32_16x16x32_bf16 v[32:35], v[164:167], v[216:219], v[32:35]
	v_exp_f32_e32 v65, v65
	v_mfma_f32_16x16x32_bf16 v[36:39], v[164:167], v[238:241], v[36:39]
	v_exp_f32_e32 v69, v69
	ds_read_b128 v[160:163], v201 offset:8192
	global_load_dwordx4 v[136:139], v196, s[6:7]
	s_waitcnt lgkmcnt(10)
	v_mfma_f32_16x16x32_bf16 v[76:79], v[168:171], v[116:119], v[76:79]
	v_exp_f32_e32 v66, v66
	v_mfma_f32_16x16x32_bf16 v[72:75], v[168:171], v[100:103], v[72:75]
	v_exp_f32_e32 v70, v70
	ds_read_b128 v[164:167], v210 offset:49152
	global_load_dwordx4 v[140:143], v197, s[6:7]
	s_waitcnt lgkmcnt(9)
	v_mfma_f32_16x16x32_bf16 v[44:47], v[172:175], v[238:241], v[44:47]
	v_exp_f32_e32 v67, v67
	v_mfma_f32_16x16x32_bf16 v[40:43], v[172:175], v[216:219], v[40:43]
	v_exp_f32_e32 v71, v71
	ds_read_b128 v[168:171], v202 offset:8192
	s_waitcnt lgkmcnt(8)
	v_mfma_f32_16x16x32_bf16 v[72:75], v[176:179], v[104:107], v[72:75]
	v_add_f32_e32 v220, v64, v65
	v_mfma_f32_16x16x32_bf16 v[76:79], v[176:179], v[120:123], v[76:79]
	v_add_f32_e32 v221, v68, v69
	ds_read_b128 v[172:175], v210 offset:51200
	s_waitcnt lgkmcnt(7)
	v_mfma_f32_16x16x32_bf16 v[48:51], v[180:183], v[216:219], v[48:51]
	v_add_f32_e32 v220, v220, v66
	v_mfma_f32_16x16x32_bf16 v[52:55], v[180:183], v[238:241], v[52:55]
	v_add_f32_e32 v221, v221, v70
	ds_read_b128 v[176:179], v203 offset:8192
	s_waitcnt lgkmcnt(6)
	v_mfma_f32_16x16x32_bf16 v[76:79], v[230:233], v[124:127], v[76:79]
	v_add_f32_e32 v220, v220, v67
	v_mfma_f32_16x16x32_bf16 v[72:75], v[230:233], v[108:111], v[72:75]
	v_add_f32_e32 v221, v221, v71
	ds_read_b128 v[180:183], v210 offset:53248
	s_waitcnt lgkmcnt(6)
	v_mfma_f32_16x16x32_bf16 v[60:63], v[234:237], v[238:241], v[60:63]
	v_mfma_f32_16x16x32_bf16 v[56:59], v[234:237], v[216:219], v[56:59]
	ds_read_b128 v[230:233], v246 offset:8192
	s_waitcnt lgkmcnt(6)
	v_mfma_f32_16x16x32_bf16 v[80:83], v[160:163], v[96:99], 0
	v_exp_f32_e32 v72, v72
	v_exp_f32_e32 v76, v76
	v_mfma_f32_16x16x32_bf16 v[84:87], v[160:163], v[112:115], 0
	v_exp_f32_e32 v73, v73
	v_exp_f32_e32 v77, v77
	ds_read_b128 v[234:237], v210 offset:55296
	s_waitcnt lgkmcnt(6)
	v_mfma_f32_16x16x32_bf16 v[0:3], v[164:167], v[242:245], v[0:3]
	v_exp_f32_e32 v74, v74
	v_exp_f32_e32 v78, v78
	v_mfma_f32_16x16x32_bf16 v[4:7], v[164:167], v[204:207], v[4:7]
	v_exp_f32_e32 v75, v75
	v_exp_f32_e32 v79, v79
	ds_read_b128 v[160:163], v201 offset:12288
	s_waitcnt lgkmcnt(6)
	v_mfma_f32_16x16x32_bf16 v[84:87], v[168:171], v[116:119], v[84:87]
	v_add_f32_e32 v220, v220, v72
	v_add_f32_e32 v221, v221, v76
	v_mfma_f32_16x16x32_bf16 v[80:83], v[168:171], v[100:103], v[80:83]
	v_add_f32_e32 v220, v220, v73
	v_add_f32_e32 v221, v221, v77
	ds_read_b128 v[164:167], v210 offset:57344
	s_waitcnt lgkmcnt(6)
	v_mfma_f32_16x16x32_bf16 v[12:15], v[172:175], v[204:207], v[12:15]
	v_add_f32_e32 v220, v220, v74
	v_add_f32_e32 v221, v221, v78
	v_mfma_f32_16x16x32_bf16 v[8:11], v[172:175], v[242:245], v[8:11]
	v_add_f32_e32 v220, v220, v75
	v_add_f32_e32 v221, v221, v79
	ds_read_b128 v[168:171], v202 offset:12288
	s_waitcnt lgkmcnt(6)
	v_mfma_f32_16x16x32_bf16 v[80:83], v[176:179], v[104:107], v[80:83]
	v_cvt_pk_bf16_f32 v216, v64, v65
	v_mfma_f32_16x16x32_bf16 v[84:87], v[176:179], v[120:123], v[84:87]
	v_cvt_pk_bf16_f32 v217, v66, v67
	ds_read_b128 v[172:175], v210 offset:59392
	s_add_u32 s10, s10, 0x200
	s_addc_u32 s11, s11, 0
	s_add_u32 s12, s12, 0x40000
	s_addc_u32 s13, s13, 0
	s_add_i32 s4, s4, 4
	s_cmpk_lt_u32 s4, 0x104
	s_cselect_b64 s[6:7], -1, 0
	s_and_b64 s[6:7], s[0:1], s[6:7]
	s_and_b64 vcc, exec, s[6:7]
	s_waitcnt lgkmcnt(6)
	v_mfma_f32_16x16x32_bf16 v[16:19], v[180:183], v[242:245], v[16:19]
	v_cvt_pk_bf16_f32 v238, v68, v69
	v_mfma_f32_16x16x32_bf16 v[20:23], v[180:183], v[204:207], v[20:23]
	v_cvt_pk_bf16_f32 v239, v70, v71
	ds_read_b128 v[176:179], v203 offset:12288
	s_waitcnt lgkmcnt(6)
	v_mfma_f32_16x16x32_bf16 v[84:87], v[230:233], v[124:127], v[84:87]
	v_cvt_pk_bf16_f32 v218, v72, v73
	v_mfma_f32_16x16x32_bf16 v[80:83], v[230:233], v[108:111], v[80:83]
	v_cvt_pk_bf16_f32 v219, v74, v75
	ds_read_b128 v[180:183], v210 offset:61440
	s_waitcnt lgkmcnt(6)
	v_mfma_f32_16x16x32_bf16 v[28:31], v[234:237], v[204:207], v[28:31]
	v_cvt_pk_bf16_f32 v240, v76, v77
	v_mfma_f32_16x16x32_bf16 v[24:27], v[234:237], v[242:245], v[24:27]
	v_cvt_pk_bf16_f32 v241, v78, v79
	ds_read_b128 v[230:233], v246 offset:12288
	s_waitcnt lgkmcnt(6)
	v_mfma_f32_16x16x32_bf16 v[88:91], v[160:163], v[96:99], 0
	v_exp_f32_e32 v80, v80
	v_mfma_f32_16x16x32_bf16 v[92:95], v[160:163], v[112:115], 0
	v_exp_f32_e32 v84, v84
	ds_read_b128 v[234:237], v210 offset:63488
	s_waitcnt lgkmcnt(6)
	v_mfma_f32_16x16x32_bf16 v[32:35], v[164:167], v[242:245], v[32:35]
	v_exp_f32_e32 v81, v81
	v_mfma_f32_16x16x32_bf16 v[36:39], v[164:167], v[204:207], v[36:39]
	v_exp_f32_e32 v85, v85
	s_waitcnt lgkmcnt(5)
	v_mfma_f32_16x16x32_bf16 v[92:95], v[168:171], v[116:119], v[92:95]
	v_exp_f32_e32 v82, v82
	v_mfma_f32_16x16x32_bf16 v[88:91], v[168:171], v[100:103], v[88:91]
	v_exp_f32_e32 v86, v86
	s_waitcnt lgkmcnt(4)
	v_mfma_f32_16x16x32_bf16 v[44:47], v[172:175], v[204:207], v[44:47]
	v_exp_f32_e32 v83, v83
	v_mfma_f32_16x16x32_bf16 v[40:43], v[172:175], v[242:245], v[40:43]
	v_exp_f32_e32 v87, v87
	s_waitcnt lgkmcnt(3)
	v_mfma_f32_16x16x32_bf16 v[88:91], v[176:179], v[104:107], v[88:91]
	v_add_f32_e32 v220, v220, v80
	v_mfma_f32_16x16x32_bf16 v[92:95], v[176:179], v[120:123], v[92:95]
	v_add_f32_e32 v221, v221, v84
	s_waitcnt lgkmcnt(2)
	v_mfma_f32_16x16x32_bf16 v[48:51], v[180:183], v[242:245], v[48:51]
	v_add_f32_e32 v220, v220, v81
	v_mfma_f32_16x16x32_bf16 v[52:55], v[180:183], v[204:207], v[52:55]
	v_add_f32_e32 v221, v221, v85
	s_waitcnt lgkmcnt(1)
	v_mfma_f32_16x16x32_bf16 v[92:95], v[230:233], v[124:127], v[92:95]
	v_add_f32_e32 v220, v220, v82
	v_mfma_f32_16x16x32_bf16 v[88:91], v[230:233], v[108:111], v[88:91]
	v_add_f32_e32 v221, v221, v86
	s_waitcnt lgkmcnt(0)
	v_mfma_f32_16x16x32_bf16 v[60:63], v[234:237], v[204:207], v[60:63]
	v_add_f32_e32 v220, v220, v83
	v_mfma_f32_16x16x32_bf16 v[56:59], v[234:237], v[242:245], v[56:59]
	v_add_f32_e32 v221, v221, v87
	s_cbranch_vccnz .LBB0_734
	s_waitcnt vmcnt(0)
	s_nop 7
	s_nop 7
	ds_swizzle_b32 v64, v194 offset:swizzle(SWAP,16)
	s_waitcnt lgkmcnt(0)
	v_add_f32_e32 v194, v194, v64
	v_mov_b32_e32 v65, v194
	s_nop 1
	v_permlane32_swap_b32_e32 v194, v65
	v_add_f32_e32 v194, v194, v65
	s_nop 0
	v_rcp_f32_e32 v66, v194
	ds_swizzle_b32 v64, v195 offset:swizzle(SWAP,16)
	s_waitcnt lgkmcnt(0)
	v_add_f32_e32 v195, v195, v64
	v_mov_b32_e32 v65, v195
	s_nop 1
	v_permlane32_swap_b32_e32 v195, v65
	v_add_f32_e32 v195, v195, v65
	s_nop 0
	v_rcp_f32_e32 v67, v195
	v_readlane_b32 s100, v250, 8
	v_mbcnt_lo_u32_b32 v68, -1, 0
	v_mbcnt_hi_u32_b32 v68, -1, v68
	v_and_b32_e32 v69, 15, v68
	v_lshrrev_b32_e32 v70, 4, v68
	s_lshr_b32 s101, s100, 1
	v_add_u32_e32 v69, s101, v69
	v_lshlrev_b32_e32 v69, 12, v69
	v_and_b32_e32 v71, 1, v70
	v_lshlrev_b32_e32 v71, 5, v71
	v_and_b32_e32 v70, 2, v70
	v_lshl_add_u32 v71, v70, 3, v71
	v_add_u32_e32 v70, v69, v71
	v_add_u32_e32 v71, 0x10000, v70
	v_mul_f32_e32 v0, v0, v66
	v_mul_f32_e32 v1, v1, v66
	v_mul_f32_e32 v2, v2, v66
	v_mul_f32_e32 v3, v3, v66
	v_mul_f32_e32 v8, v8, v66
	v_mul_f32_e32 v9, v9, v66
	v_mul_f32_e32 v10, v10, v66
	v_mul_f32_e32 v11, v11, v66
	v_cvt_pk_bf16_f32 v72, v0, v1
	v_cvt_pk_bf16_f32 v73, v2, v3
	v_cvt_pk_bf16_f32 v74, v8, v9
	v_cvt_pk_bf16_f32 v75, v10, v11
	s_nop 1
	v_permlane16_swap_b32_e32 v72, v74
	v_permlane16_swap_b32_e32 v73, v75
	s_nop 1
	global_store_dwordx4 v70, v[72:75], s[58:59] offset:0
	v_mul_f32_e32 v16, v16, v66
	v_mul_f32_e32 v17, v17, v66
	v_mul_f32_e32 v18, v18, v66
	v_mul_f32_e32 v19, v19, v66
	v_mul_f32_e32 v24, v24, v66
	v_mul_f32_e32 v25, v25, v66
	v_mul_f32_e32 v26, v26, v66
	v_mul_f32_e32 v27, v27, v66
	v_cvt_pk_bf16_f32 v76, v16, v17
	v_cvt_pk_bf16_f32 v77, v18, v19
	v_cvt_pk_bf16_f32 v78, v24, v25
	v_cvt_pk_bf16_f32 v79, v26, v27
	s_nop 1
	v_permlane16_swap_b32_e32 v76, v78
	v_permlane16_swap_b32_e32 v77, v79
	s_nop 1
	global_store_dwordx4 v70, v[76:79], s[58:59] offset:64
	v_mul_f32_e32 v32, v32, v66
	v_mul_f32_e32 v33, v33, v66
	v_mul_f32_e32 v34, v34, v66
	v_mul_f32_e32 v35, v35, v66
	v_mul_f32_e32 v40, v40, v66
	v_mul_f32_e32 v41, v41, v66
	v_mul_f32_e32 v42, v42, v66
	v_mul_f32_e32 v43, v43, v66
	v_cvt_pk_bf16_f32 v80, v32, v33
	v_cvt_pk_bf16_f32 v81, v34, v35
	v_cvt_pk_bf16_f32 v82, v40, v41
	v_cvt_pk_bf16_f32 v83, v42, v43
	s_nop 1
	v_permlane16_swap_b32_e32 v80, v82
	v_permlane16_swap_b32_e32 v81, v83
	s_nop 1
	global_store_dwordx4 v70, v[80:83], s[58:59] offset:128
	v_mul_f32_e32 v48, v48, v66
	v_mul_f32_e32 v49, v49, v66
	v_mul_f32_e32 v50, v50, v66
	v_mul_f32_e32 v51, v51, v66
	v_mul_f32_e32 v56, v56, v66
	v_mul_f32_e32 v57, v57, v66
	v_mul_f32_e32 v58, v58, v66
	v_mul_f32_e32 v59, v59, v66
	v_cvt_pk_bf16_f32 v84, v48, v49
	v_cvt_pk_bf16_f32 v85, v50, v51
	v_cvt_pk_bf16_f32 v86, v56, v57
	v_cvt_pk_bf16_f32 v87, v58, v59
	s_nop 1
	v_permlane16_swap_b32_e32 v84, v86
	v_permlane16_swap_b32_e32 v85, v87
	s_nop 1
	global_store_dwordx4 v70, v[84:87], s[58:59] offset:192
	v_mul_f32_e32 v4, v4, v67
	v_mul_f32_e32 v5, v5, v67
	v_mul_f32_e32 v6, v6, v67
	v_mul_f32_e32 v7, v7, v67
	v_mul_f32_e32 v12, v12, v67
	v_mul_f32_e32 v13, v13, v67
	v_mul_f32_e32 v14, v14, v67
	v_mul_f32_e32 v15, v15, v67
	v_cvt_pk_bf16_f32 v88, v4, v5
	v_cvt_pk_bf16_f32 v89, v6, v7
	v_cvt_pk_bf16_f32 v90, v12, v13
	v_cvt_pk_bf16_f32 v91, v14, v15
	s_nop 1
	v_permlane16_swap_b32_e32 v88, v90
	v_permlane16_swap_b32_e32 v89, v91
	s_nop 1
	global_store_dwordx4 v71, v[88:91], s[58:59] offset:0
	v_mul_f32_e32 v20, v20, v67
	v_mul_f32_e32 v21, v21, v67
	v_mul_f32_e32 v22, v22, v67
	v_mul_f32_e32 v23, v23, v67
	v_mul_f32_e32 v28, v28, v67
	v_mul_f32_e32 v29, v29, v67
	v_mul_f32_e32 v30, v30, v67
	v_mul_f32_e32 v31, v31, v67
	v_cvt_pk_bf16_f32 v92, v20, v21
	v_cvt_pk_bf16_f32 v93, v22, v23
	v_cvt_pk_bf16_f32 v94, v28, v29
	v_cvt_pk_bf16_f32 v95, v30, v31
	s_nop 1
	v_permlane16_swap_b32_e32 v92, v94
	v_permlane16_swap_b32_e32 v93, v95
	s_nop 1
	global_store_dwordx4 v71, v[92:95], s[58:59] offset:64
	v_mul_f32_e32 v36, v36, v67
	v_mul_f32_e32 v37, v37, v67
	v_mul_f32_e32 v38, v38, v67
	v_mul_f32_e32 v39, v39, v67
	v_mul_f32_e32 v44, v44, v67
	v_mul_f32_e32 v45, v45, v67
	v_mul_f32_e32 v46, v46, v67
	v_mul_f32_e32 v47, v47, v67
	v_cvt_pk_bf16_f32 v72, v36, v37
	v_cvt_pk_bf16_f32 v73, v38, v39
	v_cvt_pk_bf16_f32 v74, v44, v45
	v_cvt_pk_bf16_f32 v75, v46, v47
	s_nop 1
	v_permlane16_swap_b32_e32 v72, v74
	v_permlane16_swap_b32_e32 v73, v75
	s_nop 1
	global_store_dwordx4 v71, v[72:75], s[58:59] offset:128
	v_mul_f32_e32 v52, v52, v67
	v_mul_f32_e32 v53, v53, v67
	v_mul_f32_e32 v54, v54, v67
	v_mul_f32_e32 v55, v55, v67
	v_mul_f32_e32 v60, v60, v67
	v_mul_f32_e32 v61, v61, v67
	v_mul_f32_e32 v62, v62, v67
	v_mul_f32_e32 v63, v63, v67
	v_cvt_pk_bf16_f32 v76, v52, v53
	v_cvt_pk_bf16_f32 v77, v54, v55
	v_cvt_pk_bf16_f32 v78, v60, v61
	v_cvt_pk_bf16_f32 v79, v62, v63
	s_nop 1
	v_permlane16_swap_b32_e32 v76, v78
	v_permlane16_swap_b32_e32 v77, v79
	s_nop 1
	global_store_dwordx4 v71, v[76:79], s[58:59] offset:192
	s_barrier
